# attention LSE scratch layout residue-4-major inside a head: dilation-4 group reads/writes contiguous 64 B, dilation-16 reads at 16 B stride
# speedup vs baseline: 1.0021x; 1.0021x over previous
; #define LAS __attribute__((address_space(3)))
; #define AT_SU(s_) (2 * AT_P((s_) >> 1) + ((s_) & 1))
; #define AT_FETCH_Q(su_) do { const int su__ = (su_); const bf16* qp_ = QK + ((((size_t)((su__ >> 8) * 16 + ((su__ >> 4) & 15)) << ldil) | ((su__ >> lq4) & dilm)) * Ls + ((su__ & nq4m) * 128 + 16 * wq + n)) * 64 + 8 * kq; \
;         qf[0] = *(const bf16x8s*)qp_; qf[1] = *(const bf16x8s*)(qp_ + 32); } while (0)
; #define AT_SU(s_) (2 * AT_P((s_) >> 1) + ((s_) & 1))
; #define AT_FETCH_Q(su_) do { const int su__ = (su_); const bf16* qp_ = QK + ((((size_t)((su__ >> 8) * 16 + ((su__ >> 4) & 15)) << ldil) | ((su__ >> lq4) & dilm)) * Ls + ((su__ & nq4m) * 128 + 16 * wq + n)) * 64 + 8 * kq; \
;         qf[0] = *(const bf16x8s*)qp_; qf[1] = *(const bf16x8s*)(qp_ + 32); tick += 2; } while (0)
; __device__ __forceinline__ void attn_group_mfma5(const bf16* QK, const float* bias2g, int ldil, int first, bf16* OACC, float* LSE, LAS unsigned char* lds, const int tid, const int bid, const int G) {
;     ...
;         const int su = AT_SU(s), q4 = su & nq4m, rr = (su >> lq4) & dilm, h = (su >> 4) & 15, b = su >> 8;
;         const LAS unsigned char* Kl = lds + (s & 1) * AT5_BUF; const LAS unsigned char* Vl = Kl + 32768; const LAS float* tab = (const LAS float*)(Kl + 65536);
;         const size_t rowq = (size_t)b * SEQ + ((size_t)(q4 * 128 + 16 * wq + n) << ldil) + rr;
;         f32x4 S[9];
; #pragma unroll
;         for (int kb = 0; kb < 9; ++kb) S[kb] = (f32x4){0.f, 0.f, 0.f, 0.f};
;         { const LAS unsigned char* kp0 = Kl + (16 * wq + n) * 128;
; #pragma unroll
;           for (int ks = 0; ks < 2; ++ks)
; #pragma unroll
;             for (int kb = 0; kb < 9; ++kb) S[kb] = __builtin_amdgcn_mfma_f32_16x16x32_bf16(*(const LAS bf16x8s*)(kp0 + 16 * kb * 128 + (((4 * ks + kq) ^ fl) * 16)), qf[ks], S[kb], 0, 0, 0); }
;         __builtin_amdgcn_sched_barrier(0);
;         if (more) AT_FETCH_Q(AT_SU(s + 1));
;         float lold = 0.f; v2u xo[4];
;         if (!first) { lold = LSE[rowq * 16 + h];
; #pragma unroll
;             for (int db = 0; db < 4; ++db) xo[db] = *(const v2u*)(OACC + rowq * D + h * 64 + 16 * db + 4 * kq); }
.LBB0_215:
	s_lshl_b32 s0, s42, 1
	s_or_b32 s0, s0, s36
	s_and_b32 s36, s0, s48
	s_ashr_i32 s8, s42, 7
	s_ashr_i32 s0, s0, s39
	s_ashr_i32 s9, s8, 31
	s_lshl_b32 s36, s36, 7
	s_and_b32 s0, s0, s49
	s_lshl_b64 s[8:9], s[8:9], 11
	v_add_u32_e32 v0, s36, v71
	v_ashrrev_i32_e32 v1, 31, v0
	s_add_u32 s8, s8, s0
	s_addc_u32 s9, s9, 0
	v_lshlrev_b64 v[0:1], s43, v[0:1]
	v_lshl_add_u64 v[0:1], s[8:9], 0, v[0:1]
	v_cndmask_b32_e64 v2, 0, 1, s[44:45]
	v_and_b32_e32 v52, 0xfffff800, v0
	v_and_b32_e32 v53, 3, v0
	v_lshlrev_b32_e32 v52, 6, v52
	v_lshl_or_b32 v52, v53, 11, v52
	v_and_b32_e32 v53, 0x7fc, v0
	v_or_b32_e32 v52, v52, v53
	v_mov_b32_e32 v53, 0
	v_lshlrev_b64 v[0:1], 11, v[0:1]
	s_bfe_u32 s0, s42, 0x40003
	v_cmp_ne_u32_e64 s[8:9], 1, v2
	s_andn2_b64 vcc, exec, s[44:45]
	v_lshl_add_u64 v[62:63], s[52:53], 0, v[52:53]
	v_lshl_add_u64 v[60:61], s[46:47], 0, v[0:1]
	v_lshlrev_b32_e32 v58, 1, v50
	s_cbranch_vccnz .LBB0_217
	s_lshl_b32 s60, s0, 13
	v_lshl_add_u64 v[0:1], v[62:63], 0, s[60:61]
	s_lshl_b32 s60, s0, 7
	v_lshl_add_u64 v[52:53], v[60:61], 0, s[60:61]
	v_mov_b32_e32 v59, v3
	v_lshl_add_u64 v[52:53], v[52:53], 0, v[58:59]
	v_lshl_add_u64 v[114:115], v[52:53], 0, v[112:113]
	global_load_dword v59, v[0:1], off
	global_load_dwordx4 v[104:107], v[114:115], off
	global_load_dwordx4 v[108:111], v[114:115], off offset:64
	s_branch .LBB0_218

; #define LAS __attribute__((address_space(3)))
; #define AT_SU(s_) (2 * AT_P((s_) >> 1) + ((s_) & 1))
; #define AT_FETCH_Q(su_) do { const int su__ = (su_); const bf16* qp_ = QK + ((((size_t)((su__ >> 8) * 16 + ((su__ >> 4) & 15)) << ldil) | ((su__ >> lq4) & dilm)) * Ls + ((su__ & nq4m) * 128 + 16 * wq + n)) * 64 + 8 * kq; \
;         qf[0] = *(const bf16x8s*)qp_; qf[1] = *(const bf16x8s*)(qp_ + 32); } while (0)
; #define AT_SU(s_) (2 * AT_P((s_) >> 1) + ((s_) & 1))
; #define AT_FETCH_Q(su_) do { const int su__ = (su_); const bf16* qp_ = QK + ((((size_t)((su__ >> 8) * 16 + ((su__ >> 4) & 15)) << ldil) | ((su__ >> lq4) & dilm)) * Ls + ((su__ & nq4m) * 128 + 16 * wq + n)) * 64 + 8 * kq; \
;         qf[0] = *(const bf16x8s*)qp_; qf[1] = *(const bf16x8s*)(qp_ + 32); tick += 2; } while (0)
; __device__ __forceinline__ void attn_group_ring(const bf16* QK, const float* bias2g, int ldil, int first, bf16* OACC, float* LSE, LAS unsigned char* lds, const int tid, const int bid, const int G) {
;     ...
;         const int su = AT_SU(s), q4 = su & nq4m, rr = (su >> lq4) & dilm, h = (su >> 4) & 15, b = su >> 8;
;         const size_t rowq = (size_t)b * SEQ + ((size_t)(q4 * 128 + 16 * wq + n) << ldil) + rr;
;         f32x4 S[9];
; #pragma unroll
;         for (int kb = 0; kb < 9; ++kb) S[kb] = (f32x4){0.f, 0.f, 0.f, 0.f};
; #pragma unroll
;         for (int ks = 0; ks < 2; ++ks)
; #pragma unroll
;             for (int kb = 0; kb < 9; ++kb) { const int wrow = 16 * (wq + kb);
;                 const LAS unsigned char* kp = lds + ((a + (wrow >> 7)) & 3) * 32768 + ((wrow & 127) + n) * 128 + (((4 * ks + kq) ^ fl) * 16);
;                 S[kb] = __builtin_amdgcn_mfma_f32_16x16x32_bf16(*(const LAS bf16x8s*)kp, qf[ks], S[kb], 0, 0, 0); }
;         __builtin_amdgcn_sched_barrier(0);
;         if (more) AT_FETCH_Q(AT_SU(s + 1));
;         float lold = 0.f; v2u xo[4];
;         if (!first) { lold = LSE[rowq * 16 + h];
; #pragma unroll
;             for (int db = 0; db < 4; ++db) xo[db] = *(const v2u*)(OACC + rowq * D + h * 64 + 16 * db + 4 * kq); }
.LBB0_240:
	s_bfe_u32 s1, s87, 0x20001
	s_cmp_lt_u32 s87, 8
	s_cselect_b64 s[4:5], -1, 0
	v_cndmask_b32_e64 v0, 0, 1, s[4:5]
	v_cndmask_b32_e64 v2, 0, 1, s[6:7]
	v_readfirstlane_b32 s4, v0
	s_or_b32 s4, s49, s4
	s_lshl_b32 s5, s4, 7
	s_or_b32 s1, s5, s1
	s_or_b32 s1, s1, s45
	s_lshl_b32 s1, s1, 1
	s_and_b32 s5, s87, 1
	s_or_b32 s1, s1, s5
	s_and_b32 s70, s1, s47
	s_ashr_i32 s1, s1, s14
	s_and_b32 s71, s1, s48
	s_lshl_b32 s1, s70, 7
	s_ashr_i32 s5, s4, 31
	v_add_u32_e32 v0, s1, v64
	s_lshl_b64 s[4:5], s[4:5], 11
	v_ashrrev_i32_e32 v1, 31, v0
	s_or_b32 s4, s4, s71
	v_lshlrev_b64 v[0:1], s43, v[0:1]
	v_lshl_add_u64 v[0:1], s[4:5], 0, v[0:1]
	v_and_b32_e32 v52, 0xfffff800, v0
	v_and_b32_e32 v53, 3, v0
	v_lshlrev_b32_e32 v52, 6, v52
	v_lshl_or_b32 v52, v53, 11, v52
	v_and_b32_e32 v53, 0x7fc, v0
	v_or_b32_e32 v52, v52, v53
	v_mov_b32_e32 v53, 0
	v_lshlrev_b64 v[0:1], 11, v[0:1]
	v_cmp_ne_u32_e64 s[4:5], 1, v2
	s_andn2_b64 vcc, exec, s[6:7]
	v_lshl_add_u64 v[60:61], s[8:9], 0, v[52:53]
	v_lshl_add_u64 v[52:53], v[50:51], 0, v[0:1]
	v_lshl_add_u64 v[114:115], v[52:53], 0, v[112:113]
	s_cbranch_vccnz .LBB0_242
	global_load_dword v84, v[60:61], off
	global_load_dwordx4 v[104:107], v[114:115], off
	global_load_dwordx4 v[108:111], v[114:115], off offset:64
	s_branch .LBB0_243
